# no per-phase setprio flips + one static s_setprio 1 for waves 4-7 at kernel entry (lever 4 step a)
# speedup vs baseline: 1.0045x; 1.0014x over previous
; #define LAS __attribute__((address_space(3)))
; __device__ __forceinline__ KP kparams() { KP q = (KP)__builtin_amdgcn_kernarg_segment_ptr(); asm volatile("" : "+s"(q)); return q; }
; __global__ void __launch_bounds__(NTHR, 2) fwd(Params p_unused) {
;     extern __shared__ __attribute__((aligned(16))) unsigned char lds_raw[];
;     LAS unsigned char* lds = (LAS unsigned char*)lds_raw;
;     const int G = gridDim.x, bid = blockIdx.x;
;     const int vcu = (G % 8 == 0) ? (bid % 8) * (G / 8) + bid / 8 : bid;
;     if (threadIdx.x < 4) ((LAS unsigned*)(lds + LDS_MISC))[threadIdx.x] = 0u;
;     __syncthreads();
;     XcdBarrier bar;
;     { KP kp = kparams(); bar = xcd_barrier_post((unsigned*)(kp->ws + WS_CTL), (volatile LAS unsigned*)(lds + LDS_MISC)); }
_Z3fwd6Params:
	s_load_dword s3, s[0:1], 0x120
	s_add_u32 s4, s0, 0x120
	v_writelane_b32 v254, s0, 0
	s_addc_u32 s5, s1, 0
	s_mov_b32 s42, s2
	v_writelane_b32 v255, s2, 40
	v_readfirstlane_b32 s6, v0
	s_nop 3
	s_and_b32 s6, s6, 0x3ff
	s_lshr_b32 s6, s6, 6
	s_cmp_ge_u32 s6, 4
	s_cbranch_scc0 .Lprio_done
	s_setprio 1
.Lprio_done:
	v_writelane_b32 v254, s1, 1
	v_writelane_b32 v254, s4, 2
	s_waitcnt lgkmcnt(0)
	s_and_b32 s0, s3, 7
	s_cmp_lg_u32 s0, 0
	v_writelane_b32 v254, s5, 3
	v_writelane_b32 v254, s3, 4
	s_mov_b32 s0, s2
	s_cbranch_scc1 .LBB0_2
	s_ashr_i32 s1, s42, 31
	s_lshr_b32 s1, s1, 29
	s_add_i32 s1, s42, s1
	v_readlane_b32 s0, v254, 4
	s_ashr_i32 s2, s1, 3
	s_and_b32 s1, s1, -8
	s_ashr_i32 s0, s0, 3
	s_sub_i32 s1, s42, s1
	s_mul_i32 s0, s0, s1
	s_add_i32 s0, s0, s2
